# v12 + final_kernel kernarg hoist + scatter output-phase LDS batching (scatter preloads back after the barrier)
# speedup vs baseline: 1.0126x; 1.0126x over previous
amdhsa.kernels:
  - .agpr_count:     0
    .args:
      - .actual_access:  read_only
        .address_space:  global
        .offset:         0
        .size:           8
        .value_kind:     global_buffer
      - .address_space:  global
        .offset:         8
        .size:           8
        .value_kind:     global_buffer
      - .actual_access:  read_only
        .address_space:  global
        .offset:         16
        .size:           8
        .value_kind:     global_buffer
      - .actual_access:  read_only
        .address_space:  global
        .offset:         24
        .size:           8
        .value_kind:     global_buffer
      - .actual_access:  write_only
        .address_space:  global
        .offset:         32
        .size:           8
        .value_kind:     global_buffer
      - .actual_access:  read_only
        .address_space:  global
        .offset:         40
        .size:           8
        .value_kind:     global_buffer
      - .actual_access:  write_only
        .address_space:  global
        .offset:         48
        .size:           8
        .value_kind:     global_buffer
      - .actual_access:  write_only
        .address_space:  global
        .offset:         56
        .size:           8
        .value_kind:     global_buffer
    .group_segment_fixed_size: 6400
    .kernarg_segment_align: 8
    .kernarg_segment_size: 64
    .language:       OpenCL C
    .language_version:
      - 2
      - 0
    .max_flat_workgroup_size: 1024
    .name:           _Z17prep_count_kernelPKfPDv8_DF16_S0_S0_S2_PKiPiP15HIP_vector_typeIfLj4EE
    .private_segment_fixed_size: 0
    .sgpr_count:     22
    .sgpr_spill_count: 0
    .symbol:         _Z17prep_count_kernelPKfPDv8_DF16_S0_S0_S2_PKiPiP15HIP_vector_typeIfLj4EE.kd
    .uniform_work_group_size: 1
    .uses_dynamic_stack: false
    .vgpr_count:     22
    .vgpr_spill_count: 0
    .wavefront_size: 64
  - .agpr_count:     0
    .args:
      - .actual_access:  read_only
        .address_space:  global
        .offset:         0
        .size:           8
        .value_kind:     global_buffer
      - .actual_access:  read_only
        .address_space:  global
        .offset:         8
        .size:           8
        .value_kind:     global_buffer
      - .actual_access:  read_only
        .address_space:  global
        .offset:         16
        .size:           8
        .value_kind:     global_buffer
      - .actual_access:  write_only
        .address_space:  global
        .offset:         24
        .size:           8
        .value_kind:     global_buffer
      - .actual_access:  write_only
        .address_space:  global
        .offset:         32
        .size:           8
        .value_kind:     global_buffer
    .group_segment_fixed_size: 124704
    .kernarg_segment_align: 8
    .kernarg_segment_size: 40
    .language:       OpenCL C
    .language_version:
      - 2
      - 0
    .max_flat_workgroup_size: 1024
    .name:           _Z14scatter_kernelPKiS0_S0_PiP15HIP_vector_typeIiLj2EE
    .private_segment_fixed_size: 0
    .sgpr_count:     55
    .sgpr_spill_count: 0
    .symbol:         _Z14scatter_kernelPKiS0_S0_PiP15HIP_vector_typeIiLj2EE.kd
    .uniform_work_group_size: 1
    .uses_dynamic_stack: false
    .vgpr_count:     100
    .vgpr_spill_count: 0
    .wavefront_size: 64
  - .agpr_count:     0
    .args:
      - .actual_access:  read_only
        .address_space:  global
        .offset:         0
        .size:           8
        .value_kind:     global_buffer
      - .address_space:  global
        .offset:         8
        .size:           8
        .value_kind:     global_buffer
      - .address_space:  global
        .offset:         16
        .size:           8
        .value_kind:     global_buffer
      - .actual_access:  read_only
        .address_space:  global
        .offset:         24
        .size:           8
        .value_kind:     global_buffer
      - .actual_access:  read_only
        .address_space:  global
        .offset:         32
        .size:           8
        .value_kind:     global_buffer
      - .actual_access:  read_only
        .address_space:  global
        .offset:         40
        .size:           8
        .value_kind:     global_buffer
      - .offset:         48
        .size:           4
        .value_kind:     hidden_block_count_x
      - .offset:         52
        .size:           4
        .value_kind:     hidden_block_count_y
      - .offset:         56
        .size:           4
        .value_kind:     hidden_block_count_z
      - .offset:         60
        .size:           2
        .value_kind:     hidden_group_size_x
      - .offset:         62
        .size:           2
        .value_kind:     hidden_group_size_y
      - .offset:         64
        .size:           2
        .value_kind:     hidden_group_size_z
      - .offset:         66
        .size:           2
        .value_kind:     hidden_remainder_x
      - .offset:         68
        .size:           2
        .value_kind:     hidden_remainder_y
      - .offset:         70
        .size:           2
        .value_kind:     hidden_remainder_z
      - .offset:         88
        .size:           8
        .value_kind:     hidden_global_offset_x
      - .offset:         96
        .size:           8
        .value_kind:     hidden_global_offset_y
      - .offset:         104
        .size:           8
        .value_kind:     hidden_global_offset_z
      - .offset:         112
        .size:           2
        .value_kind:     hidden_grid_dims
    .group_segment_fixed_size: 1024
    .kernarg_segment_align: 8
    .kernarg_segment_size: 304
    .language:       OpenCL C
    .language_version:
      - 2
      - 0
    .max_flat_workgroup_size: 256
    .name:           _Z9bn_kernelPKDv8_DF16_S1_PS_PKfS4_S4_
    .private_segment_fixed_size: 0
    .sgpr_count:     20
    .sgpr_spill_count: 0
    .symbol:         _Z9bn_kernelPKDv8_DF16_S1_PS_PKfS4_S4_.kd
    .uniform_work_group_size: 1
    .uses_dynamic_stack: false
    .vgpr_count:     64
    .vgpr_spill_count: 0
    .wavefront_size: 64
  - .agpr_count:     0
    .args:
      - .actual_access:  read_only
        .address_space:  global
        .offset:         0
        .size:           8
        .value_kind:     global_buffer
      - .actual_access:  read_only
        .address_space:  global
        .offset:         8
        .size:           8
        .value_kind:     global_buffer
      - .actual_access:  read_only
        .address_space:  global
        .offset:         16
        .size:           8
        .value_kind:     global_buffer
      - .actual_access:  read_only
        .address_space:  global
        .offset:         24
        .size:           8
        .value_kind:     global_buffer
      - .actual_access:  read_only
        .address_space:  global
        .offset:         32
        .size:           8
        .value_kind:     global_buffer
      - .actual_access:  read_only
        .address_space:  global
        .offset:         40
        .size:           8
        .value_kind:     global_buffer
      - .actual_access:  read_only
        .address_space:  global
        .offset:         48
        .size:           8
        .value_kind:     global_buffer
      - .actual_access:  write_only
        .address_space:  global
        .offset:         56
        .size:           8
        .value_kind:     global_buffer
      - .offset:         64
        .size:           4
        .value_kind:     hidden_block_count_x
      - .offset:         68
        .size:           4
        .value_kind:     hidden_block_count_y
      - .offset:         72
        .size:           4
        .value_kind:     hidden_block_count_z
      - .offset:         76
        .size:           2
        .value_kind:     hidden_group_size_x
      - .offset:         78
        .size:           2
        .value_kind:     hidden_group_size_y
      - .offset:         80
        .size:           2
        .value_kind:     hidden_group_size_z
      - .offset:         82
        .size:           2
        .value_kind:     hidden_remainder_x
      - .offset:         84
        .size:           2
        .value_kind:     hidden_remainder_y
      - .offset:         86
        .size:           2
        .value_kind:     hidden_remainder_z
      - .offset:         104
        .size:           8
        .value_kind:     hidden_global_offset_x
      - .offset:         112
        .size:           8
        .value_kind:     hidden_global_offset_y
      - .offset:         120
        .size:           8
        .value_kind:     hidden_global_offset_z
      - .offset:         128
        .size:           2
        .value_kind:     hidden_grid_dims
    .group_segment_fixed_size: 34816
    .kernarg_segment_align: 8
    .kernarg_segment_size: 320
    .language:       OpenCL C
    .language_version:
      - 2
      - 0
    .max_flat_workgroup_size: 512
    .name:           _Z12final_kernelPKDv8_DF16_S1_PKfS3_S3_S1_S3_Pf
    .private_segment_fixed_size: 0
    .sgpr_count:     34
    .sgpr_spill_count: 0
    .symbol:         _Z12final_kernelPKDv8_DF16_S1_PKfS3_S3_S1_S3_Pf.kd
    .uniform_work_group_size: 1
    .uses_dynamic_stack: false
    .vgpr_count:     60
    .vgpr_spill_count: 0
    .wavefront_size: 64
  - .agpr_count:     0
    .args:
      - .actual_access:  read_only
        .address_space:  global
        .offset:         0
        .size:           8
        .value_kind:     global_buffer
      - .actual_access:  read_only
        .address_space:  global
        .offset:         8
        .size:           8
        .value_kind:     global_buffer
      - .address_space:  global
        .offset:         16
        .size:           8
        .value_kind:     global_buffer
      - .actual_access:  write_only
        .address_space:  global
        .offset:         24
        .size:           8
        .value_kind:     global_buffer
      - .address_space:  global
        .offset:         32
        .size:           8
        .value_kind:     global_buffer
      - .address_space:  global
        .offset:         40
        .size:           8
        .value_kind:     global_buffer
      - .actual_access:  read_only
        .address_space:  global
        .offset:         48
        .size:           8
        .value_kind:     global_buffer
      - .actual_access:  read_only
        .address_space:  global
        .offset:         56
        .size:           8
        .value_kind:     global_buffer
      - .address_space:  global
        .offset:         64
        .size:           8
        .value_kind:     global_buffer
      - .address_space:  global
        .offset:         72
        .size:           8
        .value_kind:     global_buffer
      - .actual_access:  read_only
        .address_space:  global
        .offset:         80
        .size:           8
        .value_kind:     global_buffer
      - .actual_access:  read_only
        .address_space:  global
        .offset:         88
        .size:           8
        .value_kind:     global_buffer
      - .offset:         96
        .size:           4
        .value_kind:     hidden_block_count_x
      - .offset:         100
        .size:           4
        .value_kind:     hidden_block_count_y
      - .offset:         104
        .size:           4
        .value_kind:     hidden_block_count_z
      - .offset:         108
        .size:           2
        .value_kind:     hidden_group_size_x
      - .offset:         110
        .size:           2
        .value_kind:     hidden_group_size_y
      - .offset:         112
        .size:           2
        .value_kind:     hidden_group_size_z
      - .offset:         114
        .size:           2
        .value_kind:     hidden_remainder_x
      - .offset:         116
        .size:           2
        .value_kind:     hidden_remainder_y
      - .offset:         118
        .size:           2
        .value_kind:     hidden_remainder_z
      - .offset:         136
        .size:           8
        .value_kind:     hidden_global_offset_x
      - .offset:         144
        .size:           8
        .value_kind:     hidden_global_offset_y
      - .offset:         152
        .size:           8
        .value_kind:     hidden_global_offset_z
      - .offset:         160
        .size:           2
        .value_kind:     hidden_grid_dims
    .group_segment_fixed_size: 26384
    .kernarg_segment_align: 8
    .kernarg_segment_size: 352
    .language:       OpenCL C
    .language_version:
      - 2
      - 0
    .max_flat_workgroup_size: 512
    .name:           _Z12layer_kernelILb1ELi512ELi64EEvPKDv8_DF16_PKfPS0_PiS6_S6_S2_S4_S5_PfPK15HIP_vector_typeIiLj2EEPKi
    .private_segment_fixed_size: 0
    .sgpr_count:     52
    .sgpr_spill_count: 0
    .symbol:         _Z12layer_kernelILb1ELi512ELi64EEvPKDv8_DF16_PKfPS0_PiS6_S6_S2_S4_S5_PfPK15HIP_vector_typeIiLj2EEPKi.kd
    .uniform_work_group_size: 1
    .uses_dynamic_stack: false
    .vgpr_count:     61
    .vgpr_spill_count: 0
    .wavefront_size: 64
  - .agpr_count:     0
    .args:
      - .actual_access:  read_only
        .address_space:  global
        .offset:         0
        .size:           8
        .value_kind:     global_buffer
      - .actual_access:  read_only
        .address_space:  global
        .offset:         8
        .size:           8
        .value_kind:     global_buffer
      - .actual_access:  read_only
        .address_space:  global
        .offset:         16
        .size:           8
        .value_kind:     global_buffer
      - .actual_access:  read_only
        .address_space:  global
        .offset:         24
        .size:           8
        .value_kind:     global_buffer
      - .actual_access:  read_only
        .address_space:  global
        .offset:         32
        .size:           8
        .value_kind:     global_buffer
      - .actual_access:  read_only
        .address_space:  global
        .offset:         40
        .size:           8
        .value_kind:     global_buffer
      - .actual_access:  read_only
        .address_space:  global
        .offset:         48
        .size:           8
        .value_kind:     global_buffer
      - .actual_access:  read_only
        .address_space:  global
        .offset:         56
        .size:           8
        .value_kind:     global_buffer
      - .address_space:  global
        .offset:         64
        .size:           8
        .value_kind:     global_buffer
      - .address_space:  global
        .offset:         72
        .size:           8
        .value_kind:     global_buffer
      - .actual_access:  read_only
        .address_space:  global
        .offset:         80
        .size:           8
        .value_kind:     global_buffer
      - .actual_access:  read_only
        .address_space:  global
        .offset:         88
        .size:           8
        .value_kind:     global_buffer
      - .offset:         96
        .size:           4
        .value_kind:     hidden_block_count_x
      - .offset:         100
        .size:           4
        .value_kind:     hidden_block_count_y
      - .offset:         104
        .size:           4
        .value_kind:     hidden_block_count_z
      - .offset:         108
        .size:           2
        .value_kind:     hidden_group_size_x
      - .offset:         110
        .size:           2
        .value_kind:     hidden_group_size_y
      - .offset:         112
        .size:           2
        .value_kind:     hidden_group_size_z
      - .offset:         114
        .size:           2
        .value_kind:     hidden_remainder_x
      - .offset:         116
        .size:           2
        .value_kind:     hidden_remainder_y
      - .offset:         118
        .size:           2
        .value_kind:     hidden_remainder_z
      - .offset:         136
        .size:           8
        .value_kind:     hidden_global_offset_x
      - .offset:         144
        .size:           8
        .value_kind:     hidden_global_offset_y
      - .offset:         152
        .size:           8
        .value_kind:     hidden_global_offset_z
      - .offset:         160
        .size:           2
        .value_kind:     hidden_grid_dims
    .group_segment_fixed_size: 12932
    .kernarg_segment_align: 8
    .kernarg_segment_size: 352
    .language:       OpenCL C
    .language_version:
      - 2
      - 0
    .max_flat_workgroup_size: 256
    .name:           _Z12layer_kernelILb0ELi256ELi32EEvPKDv8_DF16_PKfPS0_PiS6_S6_S2_S4_S5_PfPK15HIP_vector_typeIiLj2EEPKi
    .private_segment_fixed_size: 0
    .sgpr_count:     36
    .sgpr_spill_count: 0
    .symbol:         _Z12layer_kernelILb0ELi256ELi32EEvPKDv8_DF16_PKfPS0_PiS6_S6_S2_S4_S5_PfPK15HIP_vector_typeIiLj2EEPKi.kd
    .uniform_work_group_size: 1
    .uses_dynamic_stack: false
    .vgpr_count:     64
    .vgpr_spill_count: 0
    .wavefront_size: 64
